# MoE unit prologues: expert lookup by one LDS read + ballot; both token-list gathers in flight; MoE2 acquire invalidate before the tile-counter poll
# speedup vs baseline: 1.0456x; 1.0020x over previous
; template <int MODE>
; __device__ __forceinline__ int moe_gemm(const Args& a, unsigned char* lds_g, int tid, int idx0) {
;     ...
;         const int bk = w, bp = lane;
;         int e = 0;
; #pragma unroll 1
;         for (int q = 1; q < NEXP; ++q) e = (cum[q] <= ti) ? q : e;
;         e = __builtin_amdgcn_readfirstlane(e);
;         const int mt = __builtin_amdgcn_readfirstlane(ti - cum[e]);
;         unsigned aofs[4]; unsigned bofs; int bwr0;
;         __amdgpu_buffer_rsrc_t rsA, rsB, rsB3;
;         if (MODE == 1) { const int cnt = cum[128 + e];
; #pragma unroll
;             for (int q = 0; q < 2; ++q) { const int pos = 256 * mt + 128 * q + (tidu >> 2); const int tok = pos < cnt ? ((const int*)(a.ws + WS_LIST))[e * 8192 + pos] : 0;
;                 aofs[q] = (unsigned)(tok * D + 16 * (tidu & 3)); }
.LBB0_1171:
	s_mul_i32 s0, s64, s42
	s_add_i32 s38, s0, s33
	s_waitcnt lgkmcnt(0)
	v_cmp_ge_i32_e64 s[0:1], s38, v190
	s_and_b64 vcc, exec, s[0:1]
	s_cbranch_vccnz .LBB0_1170
	v_mbcnt_lo_u32_b32 v2, -1, 0
	v_mbcnt_hi_u32_b32 v2, -1, v2
	v_lshlrev_b32_e32 v0, 2, v2
	v_add_u32_e32 v0, 0x22800, v0
	ds_read_b32 v0, v0
	s_waitcnt lgkmcnt(0)
	v_cmp_ge_i32_e32 vcc, s38, v0
	s_and_b32 s6, vcc_lo, -2
	s_bcnt1_i32_b32 s6, s6
	s_lshl_b32 s7, s6, 2
	s_add_i32 s7, s7, 0
	s_add_i32 s7, s7, 0x22800
	v_mov_b32_e32 v0, s7
	ds_read2st64_b32 v[0:1], v0 offset1:2
	v_or_b32_e32 v4, s45, v2
	v_ashrrev_i32_e32 v4, 2, v4
	v_mov_b32_e32 v3, 0
	s_lshl_b32 s7, s6, 13
	s_waitcnt lgkmcnt(0)
	v_sub_u32_e32 v0, s38, v0
	s_nop 0
	v_readfirstlane_b32 s16, v0
	v_readfirstlane_b32 s8, v1
	s_lshl_b32 s9, s16, 8
	s_sub_i32 s8, s8, s9
	v_writelane_b32 v249, s8, 50
	v_mov_b32_e32 v0, 0
	s_nop 0
	v_lshl_add_u32 v4, s16, 8, v4
	v_cmp_lt_i32_e32 vcc, v4, v1
	s_and_saveexec_b64 s[16:17], vcc
	s_cbranch_execz .LBB0_1178
	v_add_u32_e32 v6, s7, v4
	v_ashrrev_i32_e32 v7, 31, v6
	v_lshl_add_u64 v[6:7], v[6:7], 2, s[28:29]
	global_load_dword v0, v[6:7], off

; #define MG_BAR() do { asm volatile("s_waitcnt lgkmcnt(0)" ::: "memory"); __builtin_amdgcn_s_barrier(); asm volatile("" ::: "memory"); } while (0)
; #define MH_LDA(te_, to_) do { ra[0] = __builtin_amdgcn_raw_buffer_load_b128(rsA, aofs[0], 64 * (te_), 0); ra[1] = __builtin_amdgcn_raw_buffer_load_b128(rsA, aofs[1], 64 * (te_), 0); \
;             ra[2] = __builtin_amdgcn_raw_buffer_load_b128(rsA, aofs[0], 64 * (to_), 0); ra[3] = __builtin_amdgcn_raw_buffer_load_b128(rsA, aofs[1], 64 * (to_), 0); } while (0)
; template <int MODE>
; __device__ __forceinline__ int moe_gemm(const Args& a, unsigned char* lds_g, int tid, int idx0) {
;     ...
;         if (MODE == 1) { const int cnt = cum[128 + e];
; #pragma unroll
;             for (int q = 0; q < 2; ++q) { const int pos = 256 * mt + 128 * q + (tidu >> 2); const int tok = pos < cnt ? ((const int*)(a.ws + WS_LIST))[e * 8192 + pos] : 0;
;                 aofs[q] = (unsigned)(tok * D + 16 * (tidu & 3)); }
;             aofs[2] = aofs[3] = 0u;
;             rsA = __builtin_amdgcn_make_buffer_rsrc((void*)(a.ws + WS_H2), 0, 0x7fffffff, 0x00020000);
;             rsB = __builtin_amdgcn_make_buffer_rsrc((void*)(a.in[I_W1] + (size_t)e * D * DE), 0, 0x7fffffff, 0x00020000); rsB3 = __builtin_amdgcn_make_buffer_rsrc((void*)(a.in[I_W3] + (size_t)e * D * DE), 0, 0x7fffffff, 0x00020000);
;             bofs = (unsigned)((bk + 8 * (bp >> 5)) * DE + 128 * nt + 4 * (bp & 31)) * 4u;
;             bwr0 = MH_BROW * (2 * (bk & 3) + (bk >> 2) + 8 * (bp >> 5)) + 2 * (128 * ((bp & 31) >> 4) + 16 * (bp & 3) + 4 * ((bp & 15) >> 2)); }
;     ...
;             MH_LDA(0, 1); MH_LDB(0);
;             MG_BAR();
.LBB0_1180:
	s_or_b64 exec, exec, s[16:17]
	s_waitcnt vmcnt(0)
	v_lshlrev_b32_e32 v0, 11, v0
	s_ashr_i32 s7, s6, 31
	v_readlane_b32 s8, v249, 6
	v_lshlrev_b32_e32 v1, 4, v2
	s_lshl_b64 s[6:7], s[6:7], 23
	v_readlane_b32 s22, v249, 20
	v_and_b32_e32 v52, 48, v1
	v_readlane_b32 s17, v249, 15
	v_readlane_b32 s23, v249, 21
	s_add_u32 s76, s22, s6
	v_or_b32_e32 v191, v3, v52
	v_readlane_b32 s20, v249, 18
	s_addc_u32 s17, s23, s7
	v_lshrrev_b32_e32 v3, 5, v2
	v_or_b32_e32 v188, v0, v52
	v_lshlrev_b32_e32 v0, 2, v2
	s_add_u32 s20, s88, s6
	v_lshlrev_b32_e32 v53, 3, v3
	v_readlane_b32 s21, v249, 19
	s_addc_u32 s6, s89, s7
	v_add_lshl_u32 v4, v53, s44, 10
	v_and_b32_e32 v5, 0x7c, v0
	v_or3_b32 v4, v4, v5, s43
	s_and_b32 s21, s6, 0xffff
	s_mov_b32 s6, s78
	s_mov_b32 s7, s79
	s_and_b32 s77, s17, 0xffff
	s_mov_b32 s22, s78
	s_mov_b32 s23, s79
	v_lshlrev_b32_e32 v192, 2, v4
	buffer_load_dwordx4 v[4:7], v188, s[4:7], 0 offen
	buffer_load_dwordx4 v[20:23], v188, s[4:7], 64 offen
	buffer_load_dwordx4 v[12:15], v191, s[4:7], 0 offen
	buffer_load_dwordx4 v[8:11], v191, s[4:7], 64 offen
	buffer_load_dwordx4 v[16:19], v192, s[76:79], 0 offen
	buffer_load_dwordx4 v[24:27], v192, s[76:79], s48 offen
	buffer_load_dwordx4 v[28:31], v192, s[20:23], 0 offen
	buffer_load_dwordx4 v[32:35], v192, s[20:23], s48 offen
	buffer_load_dwordx4 v[36:39], v192, s[76:79], s79 offen
	buffer_load_dwordx4 v[40:43], v192, s[76:79], s59 offen
	buffer_load_dwordx4 v[44:47], v192, s[20:23], s79 offen
	buffer_load_dwordx4 v[48:51], v192, s[20:23], s59 offen
	v_lshlrev_b32_e32 v54, 6, v2
	v_and_b32_e32 v55, 48, v2
	v_lshrrev_b32_e32 v56, 1, v2
	v_lshlrev_b32_e32 v57, 3, v2
	v_and_b32_e32 v58, 12, v2
	v_lshlrev_b32_e32 v59, 5, v2
	v_and_b32_e32 v60, 32, v0
	v_and_or_b32 v54, v54, s57, v55
	v_and_b32_e32 v0, 0x80, v57
	v_and_b32_e32 v55, 14, v56
	v_and_b32_e32 v1, 0x3c0, v1
	v_and_or_b32 v56, v56, 1, s50
	v_and_b32_e32 v2, 32, v2
	v_add_u32_e32 v53, s47, v53
	v_or3_b32 v0, v58, v0, v52
	v_and_or_b32 v1, v59, 32, v1
	v_lshlrev_b32_e32 v52, 10, v56
	v_lshl_or_b32 v3, v3, 4, v55
	v_mul_lo_u32 v53, v53, s58
	v_bitop3_b32 v1, v1, v52, v2 bitop3:0xde
	v_mul_u32_u24_e32 v56, 0x210, v3
	v_lshl_add_u32 v58, v0, 1, v53
	v_add_u32_e32 v193, 0, v1
	s_waitcnt lgkmcnt(0)
	s_barrier
; #define MG_BAR() do { asm volatile("s_waitcnt lgkmcnt(0)" ::: "memory"); __builtin_amdgcn_s_barrier(); asm volatile("" ::: "memory"); } while (0)
; #define MH_LDA(te_, to_) do { ra[0] = __builtin_amdgcn_raw_buffer_load_b128(rsA, aofs[0], 64 * (te_), 0); ra[1] = __builtin_amdgcn_raw_buffer_load_b128(rsA, aofs[1], 64 * (te_), 0); \
;             ra[2] = __builtin_amdgcn_raw_buffer_load_b128(rsA, aofs[0], 64 * (to_), 0); ra[3] = __builtin_amdgcn_raw_buffer_load_b128(rsA, aofs[1], 64 * (to_), 0); } while (0)
; #define MH_STB(buf_) do { _Pragma("unroll") for (int j_ = 0; j_ < 8; ++j_) { pg8::u32x2 o_; o_.x = pk2(rb[j_].x, rb[j_].y); o_.y = pk2(rb[j_].z, rb[j_].w); \
;             *(pg8::u32x2*)(lds_g + MH_B + (buf_) * MH_BBYTES + bwr0 + (MODE == 1 ? (j_ >> 1) * 16 * MH_BROW + (j_ & 1) * 128 : j_ * 8 * MH_BROW)) = o_; } } while (0)
; template <int MODE>
; __device__ __forceinline__ int moe_gemm(const Args& a, unsigned char* lds_g, int tid, int idx0) {
;     ...
;         f32x4 acc[4][8];
; #pragma unroll
;         for (int m = 0; m < 4; ++m)
; #pragma unroll
;             for (int n = 0; n < 8; ++n) acc[m][n] = (f32x4){0.f, 0.f, 0.f, 0.f};
;     ...
;             MH_LDA(0, 1); MH_LDB(0);
;             MG_BAR();
;             MH_STA(0, 0); MH_STB(0);
;             MH_LDB(1);
	v_and_b32_e32 v61, 16, v57
	s_movk_i32 s26, 0x80
	s_mov_b32 s65, 0
	v_and_b32_e32 v57, 8, v57
	v_add_u32_e32 v55, s49, v61
	v_readlane_b32 s9, v249, 7
	v_readlane_b32 s10, v249, 8
	v_readlane_b32 s11, v249, 9
	v_readlane_b32 s12, v249, 10
	v_readlane_b32 s13, v249, 11
	v_readlane_b32 s14, v249, 12
	v_readlane_b32 s15, v249, 13
	v_readlane_b32 s16, v249, 14
	v_readlane_b32 s18, v249, 16
	v_readlane_b32 s19, v249, 17
	s_waitcnt vmcnt(11)
	v_cvt_pk_f32_fp8_e32 v[0:1], v4
	v_cvt_pk_f32_fp8_sdwa v[2:3], v4 src0_sel:WORD_1
	v_cvt_pk_f32_fp8_e32 v[52:53], v5
	v_cvt_pk_f32_fp8_sdwa v[4:5], v5 src0_sel:WORD_1
	v_cvt_pk_bf16_f32 v0, v0, v1
	v_cvt_pk_bf16_f32 v1, v2, v3
	v_cvt_pk_bf16_f32 v2, v52, v53
	v_cvt_pk_bf16_f32 v3, v4, v5
	ds_write_b128 v193, v[0:3]
	v_cvt_pk_f32_fp8_e32 v[0:1], v6
	v_cvt_pk_f32_fp8_sdwa v[2:3], v6 src0_sel:WORD_1
	v_cvt_pk_f32_fp8_e32 v[4:5], v7
	v_cvt_pk_f32_fp8_sdwa v[6:7], v7 src0_sel:WORD_1
	v_cvt_pk_bf16_f32 v0, v0, v1
	v_cvt_pk_bf16_f32 v1, v2, v3
	v_cvt_pk_bf16_f32 v2, v4, v5
	v_cvt_pk_bf16_f32 v3, v6, v7
	ds_write_b128 v193, v[0:3] offset:16
	s_waitcnt vmcnt(9)
	v_cvt_pk_f32_fp8_e32 v[0:1], v12
	v_cvt_pk_f32_fp8_sdwa v[2:3], v12 src0_sel:WORD_1
	v_cvt_pk_f32_fp8_e32 v[4:5], v13
	v_cvt_pk_f32_fp8_sdwa v[6:7], v13 src0_sel:WORD_1
	v_cvt_pk_bf16_f32 v0, v0, v1
	v_cvt_pk_bf16_f32 v1, v2, v3
	v_cvt_pk_bf16_f32 v2, v4, v5
	v_cvt_pk_bf16_f32 v3, v6, v7
	ds_write_b128 v193, v[0:3] offset:16384
	v_cvt_pk_f32_fp8_e32 v[0:1], v14
	v_cvt_pk_f32_fp8_sdwa v[2:3], v14 src0_sel:WORD_1
	v_cvt_pk_f32_fp8_e32 v[4:5], v15
	v_cvt_pk_f32_fp8_sdwa v[6:7], v15 src0_sel:WORD_1
	v_cvt_pk_bf16_f32 v0, v0, v1
	v_cvt_pk_bf16_f32 v1, v2, v3
	v_cvt_pk_bf16_f32 v2, v4, v5
	v_cvt_pk_bf16_f32 v3, v6, v7
	ds_write_b128 v193, v[0:3] offset:16400
	v_add_u32_e32 v194, 0, v58
	v_add_u32_e32 v195, 0x10000, v194
	s_waitcnt vmcnt(7)
	v_cvt_pk_bf16_f32 v0, v16, v17
	v_cvt_pk_bf16_f32 v1, v18, v19
	s_waitcnt vmcnt(5)
	v_cvt_pk_bf16_f32 v2, v28, v29
	v_cvt_pk_bf16_f32 v3, v30, v31
	ds_write2_b64 v195, v[0:1], v[2:3] offset1:16
	v_cvt_pk_bf16_f32 v0, v24, v25
	v_cvt_pk_bf16_f32 v1, v26, v27
	s_waitcnt vmcnt(4)
	v_cvt_pk_bf16_f32 v2, v32, v33
	v_cvt_pk_bf16_f32 v3, v34, v35
	v_add_u32_e32 v5, 0x2000, v195
	ds_write2_b64 v5, v[0:1], v[2:3] offset0:32 offset1:48
	s_waitcnt vmcnt(3)
	v_cvt_pk_bf16_f32 v0, v36, v37
	v_cvt_pk_bf16_f32 v1, v38, v39
	s_waitcnt vmcnt(1)
	v_cvt_pk_bf16_f32 v2, v44, v45
	v_cvt_pk_bf16_f32 v3, v46, v47
	v_add_u32_e32 v5, 0x4000, v195
	ds_write2_b64 v5, v[0:1], v[2:3] offset0:64 offset1:80
	v_cvt_pk_bf16_f32 v0, v40, v41
	v_cvt_pk_bf16_f32 v1, v42, v43
	s_waitcnt vmcnt(0)
	v_cvt_pk_bf16_f32 v2, v48, v49
	v_cvt_pk_bf16_f32 v3, v50, v51
	v_add_u32_e32 v5, 0x6000, v195
	ds_write2_b64 v5, v[0:1], v[2:3] offset0:96 offset1:112
	buffer_load_dwordx4 v[124:127], v192, s[76:79], s60 offen
	buffer_load_dwordx4 v[92:95], v192, s[76:79], s61 offen
	buffer_load_dwordx4 v[120:123], v192, s[20:23], s60 offen
	buffer_load_dwordx4 v[100:103], v192, s[20:23], s61 offen
	buffer_load_dwordx4 v[104:107], v192, s[76:79], s62 offen
	buffer_load_dwordx4 v[108:111], v192, s[76:79], s63 offen
	buffer_load_dwordx4 v[112:115], v192, s[20:23], s62 offen
	buffer_load_dwordx4 v[116:119], v192, s[20:23], s63 offen
	v_bitop3_b32 v4, v54, s46, v60 bitop3:0xde
	v_mov_b32_e32 v0, 0
	v_add3_u32 v196, v55, v56, v57
	v_add_u32_e32 v197, s51, v4
	v_mov_b32_e32 v1, v0
	v_mov_b32_e32 v2, v0
	v_mov_b32_e32 v3, v0
	v_mov_b32_e32 v4, v0
	v_mov_b32_e32 v5, v0
	v_mov_b32_e32 v6, v0
	v_mov_b32_e32 v7, v0
	v_mov_b32_e32 v24, v0
	v_mov_b32_e32 v25, v0
	v_mov_b32_e32 v26, v0
	v_mov_b32_e32 v27, v0
	v_mov_b32_e32 v28, v0
	v_mov_b32_e32 v29, v0
	v_mov_b32_e32 v30, v0
	v_mov_b32_e32 v31, v0
	v_mov_b32_e32 v12, v0
	v_mov_b32_e32 v13, v0
	v_mov_b32_e32 v14, v0
	v_mov_b32_e32 v15, v0
	v_mov_b32_e32 v16, v0
	v_mov_b32_e32 v17, v0
	v_mov_b32_e32 v18, v0
	v_mov_b32_e32 v19, v0
	v_mov_b32_e32 v32, v0
	v_mov_b32_e32 v33, v0
	v_mov_b32_e32 v34, v0
	v_mov_b32_e32 v35, v0
	v_mov_b32_e32 v36, v0
	v_mov_b32_e32 v37, v0
	v_mov_b32_e32 v38, v0
	v_mov_b32_e32 v39, v0
	v_mov_b32_e32 v40, v0
	v_mov_b32_e32 v41, v0
	v_mov_b32_e32 v42, v0
	v_mov_b32_e32 v43, v0
	v_mov_b32_e32 v44, v0
	v_mov_b32_e32 v45, v0
	v_mov_b32_e32 v46, v0
	v_mov_b32_e32 v47, v0
	v_mov_b32_e32 v56, v0
	v_mov_b32_e32 v57, v0
	v_mov_b32_e32 v58, v0
	v_mov_b32_e32 v59, v0
	v_mov_b32_e32 v60, v0
	v_mov_b32_e32 v61, v0
	v_mov_b32_e32 v62, v0
	v_mov_b32_e32 v63, v0
	v_mov_b32_e32 v48, v0
	v_mov_b32_e32 v49, v0
	v_mov_b32_e32 v50, v0
	v_mov_b32_e32 v51, v0
	v_mov_b32_e32 v52, v0
	v_mov_b32_e32 v53, v0
	v_mov_b32_e32 v54, v0
	v_mov_b32_e32 v55, v0
	v_mov_b32_e32 v64, v0
	v_mov_b32_e32 v65, v0
	v_mov_b32_e32 v66, v0
	v_mov_b32_e32 v67, v0
	v_mov_b32_e32 v68, v0
	v_mov_b32_e32 v69, v0
	v_mov_b32_e32 v70, v0
	v_mov_b32_e32 v71, v0
	v_mov_b32_e32 v72, v0
	v_mov_b32_e32 v73, v0
	v_mov_b32_e32 v74, v0
	v_mov_b32_e32 v75, v0
	v_mov_b32_e32 v76, v0
	v_mov_b32_e32 v77, v0
	v_mov_b32_e32 v78, v0
	v_mov_b32_e32 v79, v0
	v_mov_b32_e32 v88, v0
	v_mov_b32_e32 v89, v0
	v_mov_b32_e32 v90, v0
	v_mov_b32_e32 v91, v0
	v_mov_b32_e32 v96, v0
	v_mov_b32_e32 v97, v0
	v_mov_b32_e32 v98, v0
	v_mov_b32_e32 v99, v0
	v_mov_b32_e32 v80, v0
	v_mov_b32_e32 v81, v0
	v_mov_b32_e32 v82, v0
	v_mov_b32_e32 v83, v0
	v_mov_b32_e32 v84, v0
	v_mov_b32_e32 v85, v0
	v_mov_b32_e32 v86, v0
	v_mov_b32_e32 v87, v0
	v_mov_b32_e32 v128, v0
	v_mov_b32_e32 v129, v0
	v_mov_b32_e32 v130, v0
	v_mov_b32_e32 v131, v0
	v_mov_b32_e32 v140, v0
	v_mov_b32_e32 v141, v0
	v_mov_b32_e32 v142, v0
	v_mov_b32_e32 v143, v0
	v_mov_b32_e32 v132, v0
	v_mov_b32_e32 v133, v0
	v_mov_b32_e32 v134, v0
	v_mov_b32_e32 v135, v0
	v_mov_b32_e32 v136, v0
	v_mov_b32_e32 v137, v0
	v_mov_b32_e32 v138, v0
	v_mov_b32_e32 v139, v0
	v_mov_b32_e32 v152, v0
	v_mov_b32_e32 v153, v0
	v_mov_b32_e32 v154, v0
	v_mov_b32_e32 v155, v0
	v_mov_b32_e32 v156, v0
	v_mov_b32_e32 v157, v0
	v_mov_b32_e32 v158, v0
	v_mov_b32_e32 v159, v0
	v_mov_b32_e32 v144, v0
	v_mov_b32_e32 v145, v0
	v_mov_b32_e32 v146, v0
	v_mov_b32_e32 v147, v0
	v_mov_b32_e32 v148, v0
	v_mov_b32_e32 v149, v0
	v_mov_b32_e32 v150, v0
	v_mov_b32_e32 v151, v0
	v_mov_b32_e32 v160, v0
	v_mov_b32_e32 v161, v0
	v_mov_b32_e32 v162, v0
	v_mov_b32_e32 v163, v0
	v_mov_b32_e32 v164, v0
	v_mov_b32_e32 v165, v0
	v_mov_b32_e32 v166, v0
	v_mov_b32_e32 v167, v0
	v_readlane_b32 s8, v249, 50
	s_lshr_b32 s9, s44, 1
	s_lshl_b32 s9, s9, 6
	s_cmp_ge_i32 s9, s8
	s_cbranch_scc1 .Lnm1_head

; __device__ __forceinline__ unsigned pk2(float lo, float hi) { return pg8::cvt_pk_bf16(lo, hi); }
; __device__ __forceinline__ int moe_pull(const Args& a, unsigned char* lds_g, int w, int x) {
;     int* slot = (int*)(lds_g + MG_CUM + 256);
;     __syncthreads();
;     if (w == 0 && fresh_lane() == 0) *slot = (int)__hip_atomic_fetch_add((unsigned*)(a.ws + WS_CTL) + CW_Q + 64 * x, 1u, __ATOMIC_RELAXED, __HIP_MEMORY_SCOPE_AGENT);
;     __syncthreads();
;     return __builtin_amdgcn_readfirstlane(*slot);
; }
; __device__ __forceinline__ unsigned f8pair_lo(unsigned w) { const auto v = __builtin_amdgcn_cvt_pk_f32_fp8((int)w, false); return pk2(v[0], v[1]); }
; __device__ __forceinline__ unsigned f8pair_hi(unsigned w) { const auto v = __builtin_amdgcn_cvt_pk_f32_fp8((int)w, true); return pk2(v[0], v[1]); }
; template <int MODE>
; __device__ __forceinline__ int moe_gemm(const Args& a, unsigned char* lds_g, int tid, int idx0) {
;     constexpr int K = MODE == 1 ? D : DE, NT = K / 64;
;     ...
;     const int w = __builtin_amdgcn_readfirstlane(tid >> 6);
;     const int wm = w >> 1, wn = w & 1, hh = wm >> 1, wr = wm & 1;
;     const int* cum = (const int*)(lds_g + MG_CUM); const unsigned* ctl = (const unsigned*)(a.ws + WS_CTL);
;     const int T = cum[NEXP], x = blockIdx.x & 7;
;     const int jl = (int)(blockIdx.x >> 3), nl = (int)(gridDim.x >> 3);
;     for (int it = 0;; ++it) {
;         int idx;
;         if (MODE == 1) idx = jl + nl * it; else idx = moe_pull(a, lds_g, w, x);
;         if (idx >= T) return idx;
;         const int ti = idx;
;         const int nt = x;
;         if (MODE == 2) {
;             if (w == 0) { unsigned* tc = (unsigned*)(a.ws + WS_CTL) + CW_TC + 64 * ti; unsigned spins = 0;
;                 while ((unsigned)__builtin_amdgcn_readfirstlane(__hip_atomic_load(tc, __ATOMIC_RELAXED, __HIP_MEMORY_SCOPE_AGENT)) < 64u) {
;                     __builtin_amdgcn_s_sleep(2);
;                     if (++spins > (1u << 22)) { if (fresh_lane() == 0) __hip_atomic_store((unsigned*)(a.ws + WS_CTL) + 1, 0x900u + (unsigned)ti, __ATOMIC_RELAXED, __HIP_MEMORY_SCOPE_AGENT); break; } }
;                 __builtin_amdgcn_fence(__ATOMIC_ACQUIRE, "agent");
;                 asm volatile("s_waitcnt vmcnt(0)" ::: "memory"); }
.LBB0_1193:
	s_waitcnt lgkmcnt(0)
	s_barrier
	ds_read_b32 v0, v191
	s_mov_b64 s[4:5], -1
	s_waitcnt lgkmcnt(0)
	v_readfirstlane_b32 s20, v0
	s_nop 1
	v_cmp_ge_i32_e32 vcc, s20, v190
	s_cbranch_vccnz .LBB0_1186
	s_and_b64 vcc, exec, s[0:1]
	s_cbranch_vccnz .LBB0_1208
	s_lshl_b32 s4, s20, 6
	s_ashr_i32 s5, s4, 31
	s_lshl_b64 s[4:5], s[4:5], 2
	s_add_u32 s4, s40, s4
	s_addc_u32 s5, s41, s5
	s_mov_b32 s21, 0x400001
	buffer_inv sc1
	s_branch .LBB0_1197

; template <int MODE>
; __device__ __forceinline__ int moe_gemm(const Args& a, unsigned char* lds_g, int tid, int idx0) {
;     ...
;             if (w == 0) { unsigned* tc = (unsigned*)(a.ws + WS_CTL) + CW_TC + 64 * ti; unsigned spins = 0;
;                 while ((unsigned)__builtin_amdgcn_readfirstlane(__hip_atomic_load(tc, __ATOMIC_RELAXED, __HIP_MEMORY_SCOPE_AGENT)) < 64u) {
;                     __builtin_amdgcn_s_sleep(2);
;                     if (++spins > (1u << 22)) { if (fresh_lane() == 0) __hip_atomic_store((unsigned*)(a.ws + WS_CTL) + 1, 0x900u + (unsigned)ti, __ATOMIC_RELAXED, __HIP_MEMORY_SCOPE_AGENT); break; } }
;                 __builtin_amdgcn_fence(__ATOMIC_ACQUIRE, "agent");
;                 asm volatile("s_waitcnt vmcnt(0)" ::: "memory"); }
;             __syncthreads();
;         }
;         const int lane = fresh_lane(), tidu = w * 64 + lane, fr = lane & 15, fq = lane >> 4;
;         const int aoff = pg8::lds_byte(wr * 64 + fr, fq * 8);
;         const int bk = w, bp = lane;
;         int e = 0;
; #pragma unroll 1
;         for (int q = 1; q < NEXP; ++q) e = (cum[q] <= ti) ? q : e;
;         e = __builtin_amdgcn_readfirstlane(e);
;         const int mt = __builtin_amdgcn_readfirstlane(ti - cum[e]);
;         unsigned aofs[4]; unsigned bofs; int bwr0;
;         __amdgpu_buffer_rsrc_t rsA, rsB, rsB3;
;         if (MODE == 1) { const int cnt = cum[128 + e];
; #pragma unroll
;             for (int q = 0; q < 2; ++q) { const int pos = 256 * mt + 128 * q + (tidu >> 2); const int tok = pos < cnt ? ((const int*)(a.ws + WS_LIST))[e * 8192 + pos] : 0;
;                 aofs[q] = (unsigned)(tok * D + 16 * (tidu & 3)); }
;             aofs[2] = aofs[3] = 0u;
;             rsA = __builtin_amdgcn_make_buffer_rsrc((void*)(a.ws + WS_H2), 0, 0x7fffffff, 0x00020000);
;             rsB = __builtin_amdgcn_make_buffer_rsrc((void*)(a.in[I_W1] + (size_t)e * D * DE), 0, 0x7fffffff, 0x00020000); rsB3 = __builtin_amdgcn_make_buffer_rsrc((void*)(a.in[I_W3] + (size_t)e * D * DE), 0, 0x7fffffff, 0x00020000);
;             bofs = (unsigned)((bk + 8 * (bp >> 5)) * DE + 128 * nt + 4 * (bp & 31)) * 4u;
;             bwr0 = MH_BROW * (2 * (bk & 3) + (bk >> 2) + 8 * (bp >> 5)) + 2 * (128 * ((bp & 31) >> 4) + 16 * (bp & 3) + 4 * ((bp & 15) >> 2)); }
;         else {
; #pragma unroll
.LBB0_1207:
	s_waitcnt vmcnt(0)
	s_waitcnt vmcnt(0)
.LBB0_1208:
	s_barrier
	v_mbcnt_lo_u32_b32 v8, -1, 0
	v_mbcnt_hi_u32_b32 v8, -1, v8
	v_lshlrev_b32_e32 v0, 2, v8
	v_add_u32_e32 v0, 0x22800, v0
	ds_read_b32 v0, v0
	s_waitcnt lgkmcnt(0)
	v_cmp_ge_i32_e32 vcc, s20, v0
	s_and_b32 s4, vcc_lo, -2
	s_bcnt1_i32_b32 s4, s4
	s_ashr_i32 s21, s20, 31
	s_ashr_i32 s5, s4, 31
	s_lshl_b64 s[16:17], s[20:21], 18
	s_add_u32 s16, s2, s16
	v_or_b32_e32 v1, s22, v8
	s_waitcnt vmcnt(18)
	v_lshlrev_b32_e32 v50, 4, v8
	s_addc_u32 s17, s3, s17
	s_lshl_b64 s[4:5], s[4:5], 23
	v_lshlrev_b32_e32 v9, 2, v8
	v_lshlrev_b32_e32 v0, 8, v1
	v_and_b32_e32 v1, 48, v50
	s_add_u32 s4, s90, s4
	v_and_or_b32 v188, v0, s42, v1
	s_addc_u32 s5, s91, s5
	v_or_b32_e32 v0, s26, v9
	s_and_b32 s17, s17, 0xffff
	s_mov_b32 s18, s6
	s_mov_b32 s19, s7
	v_add_u32_e32 v192, 0x20000, v188
	s_and_b32 s5, s5, 0xffff
	v_lshlrev_b32_e32 v193, 2, v0
	buffer_load_dwordx4 v[10:13], v188, s[16:19], 0 offen
	buffer_load_dwordx4 v[4:7], v188, s[16:19], 64 offen
	buffer_load_dwordx4 v[14:17], v192, s[16:19], 0 offen
	buffer_load_dwordx4 v[0:3], v192, s[16:19], 64 offen
	buffer_load_dwordx4 v[18:21], v193, s[4:7], 0 offen
	buffer_load_dwordx4 v[22:25], v193, s[4:7], s28 offen
	buffer_load_dwordx4 v[26:29], v193, s[4:7], s7 offen
	buffer_load_dwordx4 v[30:33], v193, s[4:7], s43 offen
	buffer_load_dwordx4 v[34:37], v193, s[4:7], s44 offen
	buffer_load_dwordx4 v[38:41], v193, s[4:7], s45 offen
	buffer_load_dwordx4 v[42:45], v193, s[4:7], s46 offen
	buffer_load_dwordx4 v[46:49], v193, s[4:7], s47 offen
	s_waitcnt vmcnt(29)
	v_lshrrev_b32_e32 v53, 1, v8
	v_lshlrev_b32_e32 v51, 6, v8
	v_and_b32_e32 v52, 48, v8
	v_lshrrev_b32_e32 v54, 5, v8
	v_lshlrev_b32_e32 v55, 3, v8
	s_waitcnt vmcnt(28)
	v_lshlrev_b32_e32 v57, 5, v8
	v_and_b32_e32 v61, 14, v53
	v_and_b32_e32 v50, 0x3c0, v50
	v_and_or_b32 v53, v53, 1, s30
	v_and_b32_e32 v56, 1, v8
	v_and_b32_e32 v8, 32, v8
	v_and_or_b32 v59, v51, s39, v52
	v_lshlrev_b32_e32 v51, 8, v54
	v_and_b32_e32 v52, 0xc0, v55
	v_and_or_b32 v50, v57, 32, v50
	v_lshlrev_b32_e32 v53, 10, v53
	v_and_b32_e32 v58, 32, v9
	v_lshlrev_b32_e32 v60, 5, v56
	v_and_b32_e32 v55, 16, v55
	v_and_b32_e32 v9, 24, v9
	v_add3_u32 v51, v52, s27, v51
	v_lshl_or_b32 v52, v54, 4, v61
	v_bitop3_b32 v8, v50, v53, v8 bitop3:0xde
	v_lshlrev_b32_e32 v62, 3, v56
	v_add_u32_e32 v61, s29, v55
	v_mul_u32_u24_e32 v63, 0x210, v52
	v_add3_u32 v56, v51, v60, v9
	v_add_u32_e32 v194, 0, v8
	s_waitcnt lgkmcnt(0)
	s_barrier
; #define MG_BAR() do { asm volatile("s_waitcnt lgkmcnt(0)" ::: "memory"); __builtin_amdgcn_s_barrier(); asm volatile("" ::: "memory"); } while (0)
; #define MH_LDA(te_, to_) do { ra[0] = __builtin_amdgcn_raw_buffer_load_b128(rsA, aofs[0], 64 * (te_), 0); ra[1] = __builtin_amdgcn_raw_buffer_load_b128(rsA, aofs[1], 64 * (te_), 0); \
;             ra[2] = __builtin_amdgcn_raw_buffer_load_b128(rsA, aofs[0], 64 * (to_), 0); ra[3] = __builtin_amdgcn_raw_buffer_load_b128(rsA, aofs[1], 64 * (to_), 0); } while (0)
; #define MH_STB(buf_) do { _Pragma("unroll") for (int j_ = 0; j_ < 8; ++j_) { pg8::u32x2 o_; o_.x = pk2(rb[j_].x, rb[j_].y); o_.y = pk2(rb[j_].z, rb[j_].w); \
;             *(pg8::u32x2*)(lds_g + MH_B + (buf_) * MH_BBYTES + bwr0 + (MODE == 1 ? (j_ >> 1) * 16 * MH_BROW + (j_ & 1) * 128 : j_ * 8 * MH_BROW)) = o_; } } while (0)
; template <int MODE>
; __device__ __forceinline__ int moe_gemm(const Args& a, unsigned char* lds_g, int tid, int idx0) {
;     ...
;         f32x4 acc[4][8];
; #pragma unroll
;         for (int m = 0; m < 4; ++m)
; #pragma unroll
;             for (int n = 0; n < 8; ++n) acc[m][n] = (f32x4){0.f, 0.f, 0.f, 0.f};
;     ...
;             MH_LDA(0, 1); MH_LDB(0);
;             MG_BAR();
;             MH_STA(0, 0); MH_STB(0);
;             MH_LDB(1);
	s_mov_b32 s18, 0
	s_waitcnt vmcnt(11)
	v_cvt_pk_f32_fp8_e32 v[8:9], v10
	v_cvt_pk_f32_fp8_sdwa v[50:51], v10 src0_sel:WORD_1
	v_cvt_pk_f32_fp8_e32 v[52:53], v11
	v_cvt_pk_f32_fp8_sdwa v[54:55], v11 src0_sel:WORD_1
	v_cvt_pk_bf16_f32 v8, v8, v9
	v_cvt_pk_bf16_f32 v9, v50, v51
	v_cvt_pk_bf16_f32 v10, v52, v53
	v_cvt_pk_bf16_f32 v11, v54, v55
	ds_write_b128 v194, v[8:11]
	v_cvt_pk_f32_fp8_e32 v[8:9], v12
	v_cvt_pk_f32_fp8_sdwa v[10:11], v12 src0_sel:WORD_1
	v_cvt_pk_f32_fp8_e32 v[50:51], v13
	v_cvt_pk_f32_fp8_sdwa v[12:13], v13 src0_sel:WORD_1
	v_cvt_pk_bf16_f32 v8, v8, v9
	v_cvt_pk_bf16_f32 v9, v10, v11
	v_cvt_pk_bf16_f32 v10, v50, v51
	v_cvt_pk_bf16_f32 v11, v12, v13
	ds_write_b128 v194, v[8:11] offset:16
	s_waitcnt vmcnt(9)
	v_cvt_pk_f32_fp8_e32 v[8:9], v14
	v_cvt_pk_f32_fp8_sdwa v[10:11], v14 src0_sel:WORD_1
	v_cvt_pk_f32_fp8_e32 v[12:13], v15
	v_cvt_pk_f32_fp8_sdwa v[14:15], v15 src0_sel:WORD_1
	v_cvt_pk_bf16_f32 v8, v8, v9
	v_cvt_pk_bf16_f32 v9, v10, v11
	v_cvt_pk_bf16_f32 v10, v12, v13
	v_cvt_pk_bf16_f32 v11, v14, v15
	ds_write_b128 v194, v[8:11] offset:16384
	v_cvt_pk_f32_fp8_e32 v[8:9], v16
	v_cvt_pk_f32_fp8_sdwa v[10:11], v16 src0_sel:WORD_1
	v_cvt_pk_f32_fp8_e32 v[12:13], v17
	v_cvt_pk_f32_fp8_sdwa v[14:15], v17 src0_sel:WORD_1
	v_cvt_pk_bf16_f32 v8, v8, v9
	v_cvt_pk_bf16_f32 v9, v10, v11
	v_cvt_pk_bf16_f32 v10, v12, v13
	v_cvt_pk_bf16_f32 v11, v14, v15
	ds_write_b128 v194, v[8:11] offset:16400
	v_add_u32_e32 v195, 0, v56
	v_add_u32_e32 v196, 0x10000, v195
	s_waitcnt vmcnt(7)
	v_cvt_pk_bf16_f32 v8, v18, v19
	v_cvt_pk_bf16_f32 v9, v20, v21
	ds_write_b64 v196, v[8:9]
	s_waitcnt vmcnt(6)
	v_cvt_pk_bf16_f32 v8, v22, v23
	v_cvt_pk_bf16_f32 v9, v24, v25
	ds_write_b64 v196, v[8:9] offset:4224
	s_waitcnt vmcnt(5)
	v_cvt_pk_bf16_f32 v8, v26, v27
	v_cvt_pk_bf16_f32 v9, v28, v29
	ds_write_b64 v196, v[8:9] offset:8448
	s_waitcnt vmcnt(4)
	v_cvt_pk_bf16_f32 v8, v30, v31
	v_cvt_pk_bf16_f32 v9, v32, v33
	ds_write_b64 v196, v[8:9] offset:12672
	s_waitcnt vmcnt(3)
	v_cvt_pk_bf16_f32 v8, v34, v35
	v_cvt_pk_bf16_f32 v9, v36, v37
	ds_write_b64 v196, v[8:9] offset:16896
	s_waitcnt vmcnt(2)
	v_cvt_pk_bf16_f32 v8, v38, v39
	v_cvt_pk_bf16_f32 v9, v40, v41
	ds_write_b64 v196, v[8:9] offset:21120
	s_waitcnt vmcnt(1)
	v_cvt_pk_bf16_f32 v8, v42, v43
	v_cvt_pk_bf16_f32 v9, v44, v45
	ds_write_b64 v196, v[8:9] offset:25344
	s_waitcnt vmcnt(0)
	v_cvt_pk_bf16_f32 v8, v46, v47
	v_cvt_pk_bf16_f32 v9, v48, v49
	ds_write_b64 v196, v[8:9] offset:29568
	v_bitop3_b32 v10, v59, s23, v58 bitop3:0xde
	buffer_load_dwordx4 v[68:71], v193, s[4:7], s48 offen
	buffer_load_dwordx4 v[64:67], v193, s[4:7], s49 offen
	buffer_load_dwordx4 v[36:39], v193, s[4:7], s50 offen
	buffer_load_dwordx4 v[40:43], v193, s[4:7], s51 offen
	buffer_load_dwordx4 v[44:47], v193, s[4:7], s52 offen
	buffer_load_dwordx4 v[48:51], v193, s[4:7], s53 offen
	buffer_load_dwordx4 v[52:55], v193, s[4:7], s54 offen
	buffer_load_dwordx4 v[56:59], v193, s[4:7], s55 offen
	v_mov_b32_e32 v8, 0
	v_add3_u32 v197, v61, v63, v62
	s_movk_i32 s58, 0x80
	v_add_u32_e32 v198, s31, v10
	v_mov_b32_e32 v9, v8
	v_mov_b32_e32 v10, v8
	v_mov_b32_e32 v11, v8
	v_mov_b32_e32 v12, v8
	v_mov_b32_e32 v13, v8
	v_mov_b32_e32 v14, v8
	v_mov_b32_e32 v15, v8
	v_mov_b32_e32 v16, v8
	v_mov_b32_e32 v17, v8
	v_mov_b32_e32 v18, v8
	v_mov_b32_e32 v19, v8
	v_mov_b32_e32 v20, v8
	v_mov_b32_e32 v21, v8
	v_mov_b32_e32 v22, v8
	v_mov_b32_e32 v23, v8
	v_mov_b32_e32 v24, v8
	v_mov_b32_e32 v25, v8
	v_mov_b32_e32 v26, v8
	v_mov_b32_e32 v27, v8
	v_mov_b32_e32 v28, v8
	v_mov_b32_e32 v29, v8
	v_mov_b32_e32 v30, v8
	v_mov_b32_e32 v31, v8
	v_mov_b32_e32 v80, v8
	v_mov_b32_e32 v81, v8
	v_mov_b32_e32 v82, v8
	v_mov_b32_e32 v83, v8
	v_mov_b32_e32 v84, v8
	v_mov_b32_e32 v85, v8
	v_mov_b32_e32 v86, v8
	v_mov_b32_e32 v87, v8
	v_mov_b32_e32 v32, v8
	v_mov_b32_e32 v33, v8
	v_mov_b32_e32 v34, v8
	v_mov_b32_e32 v35, v8
	v_mov_b32_e32 v60, v8
	v_mov_b32_e32 v61, v8
	v_mov_b32_e32 v62, v8
	v_mov_b32_e32 v63, v8
	v_mov_b32_e32 v72, v8
	v_mov_b32_e32 v73, v8
	v_mov_b32_e32 v74, v8
	v_mov_b32_e32 v75, v8
	v_mov_b32_e32 v76, v8
	v_mov_b32_e32 v77, v8
	v_mov_b32_e32 v78, v8
	v_mov_b32_e32 v79, v8
	v_mov_b32_e32 v88, v8
	v_mov_b32_e32 v89, v8
	v_mov_b32_e32 v90, v8
	v_mov_b32_e32 v91, v8
	v_mov_b32_e32 v92, v8
	v_mov_b32_e32 v93, v8
	v_mov_b32_e32 v94, v8
	v_mov_b32_e32 v95, v8
	v_mov_b32_e32 v108, v8
	v_mov_b32_e32 v109, v8
	v_mov_b32_e32 v110, v8
	v_mov_b32_e32 v111, v8
	v_mov_b32_e32 v116, v8
	v_mov_b32_e32 v117, v8
	v_mov_b32_e32 v118, v8
	v_mov_b32_e32 v119, v8
	v_mov_b32_e32 v96, v8
	v_mov_b32_e32 v97, v8
	v_mov_b32_e32 v98, v8
	v_mov_b32_e32 v99, v8
	v_mov_b32_e32 v100, v8
	v_mov_b32_e32 v101, v8
	v_mov_b32_e32 v102, v8
	v_mov_b32_e32 v103, v8
	v_mov_b32_e32 v104, v8
	v_mov_b32_e32 v105, v8
	v_mov_b32_e32 v106, v8
	v_mov_b32_e32 v107, v8
	v_mov_b32_e32 v112, v8
	v_mov_b32_e32 v113, v8
	v_mov_b32_e32 v114, v8
	v_mov_b32_e32 v115, v8
	v_mov_b32_e32 v120, v8
	v_mov_b32_e32 v121, v8
	v_mov_b32_e32 v122, v8
	v_mov_b32_e32 v123, v8
	v_mov_b32_e32 v132, v8
	v_mov_b32_e32 v133, v8
	v_mov_b32_e32 v134, v8
	v_mov_b32_e32 v135, v8
	v_mov_b32_e32 v144, v8
	v_mov_b32_e32 v145, v8
	v_mov_b32_e32 v146, v8
	v_mov_b32_e32 v147, v8
	v_mov_b32_e32 v148, v8
	v_mov_b32_e32 v149, v8
	v_mov_b32_e32 v150, v8
	v_mov_b32_e32 v151, v8
	v_mov_b32_e32 v124, v8
	v_mov_b32_e32 v125, v8
	v_mov_b32_e32 v126, v8
	v_mov_b32_e32 v127, v8
	v_mov_b32_e32 v128, v8
	v_mov_b32_e32 v129, v8
	v_mov_b32_e32 v130, v8
	v_mov_b32_e32 v131, v8
	v_mov_b32_e32 v136, v8
	v_mov_b32_e32 v137, v8
	v_mov_b32_e32 v138, v8
	v_mov_b32_e32 v139, v8
	v_mov_b32_e32 v140, v8
	v_mov_b32_e32 v141, v8
	v_mov_b32_e32 v142, v8
	v_mov_b32_e32 v143, v8
	v_mov_b32_e32 v152, v8
	v_mov_b32_e32 v153, v8
	v_mov_b32_e32 v154, v8
	v_mov_b32_e32 v155, v8
	v_mov_b32_e32 v156, v8
	v_mov_b32_e32 v157, v8
	v_mov_b32_e32 v158, v8
	v_mov_b32_e32 v159, v8
	v_mov_b32_e32 v160, v8
	v_mov_b32_e32 v161, v8
	v_mov_b32_e32 v162, v8
	v_mov_b32_e32 v163, v8
	v_mov_b32_e32 v164, v8
	v_mov_b32_e32 v165, v8
	v_mov_b32_e32 v166, v8
	v_mov_b32_e32 v167, v8
